# baseline (speedup 1.0000x reference)
_Z5k_aggPKDF16_PKhPKiS4_PKDv8_DF16_PKfPDF16_Pf:
	s_load_dwordx8 s[4:11], s[0:1], 0x8
	s_load_dwordx4 s[12:15], s[0:1], 0x28
	s_load_dwordx2 s[16:17], s[0:1], 0x38
	v_lshlrev_b32_e32 v2, 4, v0
	s_lshl_b32 s0, s2, 2
	s_lshl_b32 s1, s2, 3
	s_andn2_b32 s0, s0, 63
	s_and_b32 s1, s1, 56
	s_or_b32 s0, s0, s1
	s_lshr_b32 s1, s2, 1
	s_and_b32 s1, s1, 4
	s_or_b32 s0, s0, s1
	v_lshlrev_b32_e32 v1, 2, v0
	v_lshrrev_b32_e32 v52, 6, v0
	v_or_b32_e32 v3, s0, v52
	v_mov_b32_e32 v98, v2
	s_waitcnt lgkmcnt(0)
	v_readfirstlane_b32 s19, v52
	s_nop 3
	s_lshl_b32 s19, s19, 10
	s_mov_b32 m0, s19
	s_nop 0
	global_load_lds_dwordx4 v2, s[10:11]
	s_add_u32 m0, s19, 0x1000
	v_add_u32_e32 v96, 0x1000, v2
	global_load_lds_dwordx4 v96, s[10:11]
	s_add_u32 m0, s19, 0x2000
	v_add_u32_e32 v96, 0x2000, v2
	global_load_lds_dwordx4 v96, s[10:11]
	s_add_u32 m0, s19, 0x3000
	v_add_u32_e32 v96, 0x3000, v2
	global_load_lds_dwordx4 v96, s[10:11]
	s_add_u32 m0, s19, 0x4000
	v_add_u32_e32 v96, 0x4000, v2
	global_load_lds_dwordx4 v96, s[10:11]
	s_add_u32 m0, s19, 0x5000
	v_add_u32_e32 v96, 0x5000, v2
	global_load_lds_dwordx4 v96, s[10:11]
	s_add_u32 m0, s19, 0x6000
	v_add_u32_e32 v96, 0x6000, v2
	global_load_lds_dwordx4 v96, s[10:11]
	s_add_u32 m0, s19, 0x7000
	v_add_u32_e32 v96, 0x7000, v2
	global_load_lds_dwordx4 v96, s[10:11]
	v_mov_b32_e32 v97, 0
	ds_write2st64_b32 v1, v97, v97 offset0:128 offset1:132
	ds_write2st64_b32 v1, v97, v97 offset0:136 offset1:140
	s_movk_i32 s0, 0x186a
	v_cmp_gt_i32_e32 vcc, s0, v3
	s_and_saveexec_b64 s[0:1], vcc
	s_cbranch_execz .Lagg_invalid
	v_bfe_u32 v4, v0, 2, 4
	v_lshlrev_b32_e32 v53, 4, v3
	v_or_b32_e32 v10, v53, v4
	v_and_b32_e32 v54, 48, v2
	v_lshl_or_b32 v11, v10, 7, v54
	global_load_dwordx4 v[2:5], v11, s[4:5]
	global_load_dwordx4 v[6:9], v11, s[4:5] offset:64
	v_ashrrev_i32_e32 v11, 31, v10
	v_lshl_add_u64 v[10:11], v[10:11], 2, s[6:7]
	global_load_dwordx2 v[50:51], v[10:11], off
	s_waitcnt vmcnt(2)
	v_cvt_pk_f32_fp8_e32 v[10:11], v2
	v_cvt_pk_f32_fp8_sdwa v[12:13], v2 src0_sel:WORD_1
	v_cvt_pk_f32_fp8_e32 v[14:15], v3
	v_cvt_pk_f32_fp8_sdwa v[2:3], v3 src0_sel:WORD_1
	v_cvt_pk_f32_fp8_e32 v[16:17], v4
	v_cvt_pk_f32_fp8_sdwa v[18:19], v4 src0_sel:WORD_1
	v_cvt_pk_f32_fp8_e32 v[20:21], v5
	v_cvt_pk_f32_fp8_sdwa v[4:5], v5 src0_sel:WORD_1
	s_waitcnt vmcnt(1)
	v_cvt_pk_f32_fp8_e32 v[22:23], v6
	v_cvt_pk_f32_fp8_sdwa v[24:25], v6 src0_sel:WORD_1
	v_cvt_pk_f32_fp8_e32 v[26:27], v7
	v_cvt_pk_f32_fp8_sdwa v[6:7], v7 src0_sel:WORD_1
	v_cvt_pk_f32_fp8_e32 v[28:29], v8
	v_cvt_pk_f32_fp8_sdwa v[30:31], v8 src0_sel:WORD_1
	v_cvt_pk_f32_fp8_e32 v[32:33], v9
	v_cvt_pk_f32_fp8_sdwa v[8:9], v9 src0_sel:WORD_1
	v_add_f32_e32 v88, 0, v10
	v_add_f32_e32 v89, 0, v11
	v_add_f32_e32 v90, 0, v12
	v_add_f32_e32 v91, 0, v13
	v_add_f32_e32 v92, 0, v14
	v_add_f32_e32 v93, 0, v15
	v_add_f32_e32 v94, 0, v2
	v_add_f32_e32 v95, 0, v3
	v_add_f32_e32 v76, 0, v16
	v_add_f32_e32 v77, 0, v17
	v_add_f32_e32 v80, 0, v18
	v_add_f32_e32 v81, 0, v19
	v_add_f32_e32 v84, 0, v20
	v_add_f32_e32 v85, 0, v21
	v_add_f32_e32 v86, 0, v4
	v_add_f32_e32 v87, 0, v5
	v_add_f32_e32 v72, 0, v22
	v_add_f32_e32 v73, 0, v23
	v_add_f32_e32 v74, 0, v24
	v_add_f32_e32 v75, 0, v25
	v_add_f32_e32 v78, 0, v26
	v_add_f32_e32 v79, 0, v27
	v_add_f32_e32 v82, 0, v6
	v_add_f32_e32 v83, 0, v7
	v_add_f32_e32 v64, 0, v28
	v_add_f32_e32 v65, 0, v29
	v_add_f32_e32 v66, 0, v30
	v_add_f32_e32 v67, 0, v31
	v_add_f32_e32 v68, 0, v32
	v_add_f32_e32 v69, 0, v33
	v_add_f32_e32 v70, 0, v8
	v_add_f32_e32 v71, 0, v9
	s_waitcnt vmcnt(0)
	s_mov_b64 s[6:7], exec
	v_add_u32_e32 v55, -1, v51
	v_max_i32_e32 v55, 0, v55
	v_mov_b32_e32 v62, 0xc35000
	v_add_u32_e32 v104, 0, v50
	v_min_i32_e32 v104, v104, v55
	v_lshlrev_b32_e32 v104, 2, v104
	global_load_dword v56, v104, s[8:9]
	v_add_u32_e32 v104, 1, v50
	v_min_i32_e32 v104, v104, v55
	v_lshlrev_b32_e32 v104, 2, v104
	global_load_dword v57, v104, s[8:9]
	v_add_u32_e32 v104, 2, v50
	v_min_i32_e32 v104, v104, v55
	v_lshlrev_b32_e32 v104, 2, v104
	global_load_dword v58, v104, s[8:9]
	v_add_u32_e32 v104, 3, v50
	v_min_i32_e32 v104, v104, v55
	v_lshlrev_b32_e32 v104, 2, v104
	global_load_dword v59, v104, s[8:9]
	v_add_u32_e32 v104, 4, v50
	v_min_i32_e32 v104, v104, v55
	v_lshlrev_b32_e32 v104, 2, v104
	global_load_dword v60, v104, s[8:9]
	v_add_u32_e32 v104, 5, v50
	v_min_i32_e32 v104, v104, v55
	v_lshlrev_b32_e32 v104, 2, v104
	global_load_dword v61, v104, s[8:9]
	s_waitcnt vmcnt(0)
	v_add_u32_e32 v104, 0, v50
	v_cmp_lt_i32_e32 vcc, v104, v51
	v_lshlrev_b32_e32 v105, 7, v56
	v_add_u32_e32 v106, 6, v104
	v_min_i32_e32 v106, v106, v55
	v_cndmask_b32_e32 v105, v62, v105, vcc
	v_or_b32_e32 v105, v54, v105
	global_load_dwordx4 v[2:5], v105, s[4:5]
	global_load_dwordx4 v[6:9], v105, s[4:5] offset:64
	v_lshlrev_b32_e32 v106, 2, v106
	global_load_dword v56, v106, s[8:9]
	v_add_u32_e32 v104, 1, v50
	v_cmp_lt_i32_e32 vcc, v104, v51
	v_lshlrev_b32_e32 v105, 7, v57
	v_add_u32_e32 v106, 6, v104
	v_min_i32_e32 v106, v106, v55
	v_cndmask_b32_e32 v105, v62, v105, vcc
	v_or_b32_e32 v105, v54, v105
	global_load_dwordx4 v[10:13], v105, s[4:5]
	global_load_dwordx4 v[14:17], v105, s[4:5] offset:64
	v_lshlrev_b32_e32 v106, 2, v106
	global_load_dword v57, v106, s[8:9]
	v_add_u32_e32 v104, 2, v50
	v_cmp_lt_i32_e32 vcc, v104, v51
	v_lshlrev_b32_e32 v105, 7, v58
	v_add_u32_e32 v106, 6, v104
	v_min_i32_e32 v106, v106, v55
	v_cndmask_b32_e32 v105, v62, v105, vcc
	v_or_b32_e32 v105, v54, v105
	global_load_dwordx4 v[18:21], v105, s[4:5]
	global_load_dwordx4 v[22:25], v105, s[4:5] offset:64
	v_lshlrev_b32_e32 v106, 2, v106
	global_load_dword v58, v106, s[8:9]
	v_add_u32_e32 v104, 3, v50
	v_cmp_lt_i32_e32 vcc, v104, v51
	v_lshlrev_b32_e32 v105, 7, v59
	v_add_u32_e32 v106, 6, v104
	v_min_i32_e32 v106, v106, v55
	v_cndmask_b32_e32 v105, v62, v105, vcc
	v_or_b32_e32 v105, v54, v105
	global_load_dwordx4 v[26:29], v105, s[4:5]
	global_load_dwordx4 v[30:33], v105, s[4:5] offset:64
	v_lshlrev_b32_e32 v106, 2, v106
	global_load_dword v59, v106, s[8:9]
	v_add_u32_e32 v104, 4, v50
	v_cmp_lt_i32_e32 vcc, v104, v51
	v_lshlrev_b32_e32 v105, 7, v60
	v_add_u32_e32 v106, 6, v104
	v_min_i32_e32 v106, v106, v55
	v_cndmask_b32_e32 v105, v62, v105, vcc
	v_or_b32_e32 v105, v54, v105
	global_load_dwordx4 v[34:37], v105, s[4:5]
	global_load_dwordx4 v[38:41], v105, s[4:5] offset:64
	v_lshlrev_b32_e32 v106, 2, v106
	global_load_dword v60, v106, s[8:9]
	v_add_u32_e32 v104, 5, v50
	v_cmp_lt_i32_e32 vcc, v104, v51
	v_lshlrev_b32_e32 v105, 7, v61
	v_add_u32_e32 v106, 6, v104
	v_min_i32_e32 v106, v106, v55
	v_cndmask_b32_e32 v105, v62, v105, vcc
	v_or_b32_e32 v105, v54, v105
	global_load_dwordx4 v[42:45], v105, s[4:5]
	global_load_dwordx4 v[46:49], v105, s[4:5] offset:64
	v_lshlrev_b32_e32 v106, 2, v106
	global_load_dword v61, v106, s[8:9]

.Lagg_invalid:
	s_or_b64 exec, exec, s[0:1]
	s_waitcnt vmcnt(0)
	s_waitcnt lgkmcnt(0)
	s_barrier
	s_branch .LBB2_8

.LBB4_2:
	s_or_b64 exec, exec, s[20:21]
	v_lshlrev_b32_e32 v18, 4, v0
	s_waitcnt lgkmcnt(0)
	v_readfirstlane_b32 s23, v62
	s_nop 3
	s_lshl_b32 s23, s23, 10
	s_mov_b32 m0, s23
	s_nop 0
	global_load_lds_dwordx4 v18, s[4:5]
	s_add_u32 m0, s23, 0x2000
	v_add_u32_e32 v19, 0x2000, v18
	global_load_lds_dwordx4 v19, s[4:5]
	s_add_u32 m0, s23, 0x4000
	v_add_u32_e32 v19, 0x4000, v18
	global_load_lds_dwordx4 v19, s[4:5]
	s_add_u32 m0, s23, 0x6000
	v_add_u32_e32 v19, 0x6000, v18
	global_load_lds_dwordx4 v19, s[4:5]
	v_lshlrev_b32_e32 v18, 2, v0
	v_or_b32_e32 v1, 0x8000, v18
	v_mov_b32_e32 v19, 0
	s_mov_b64 s[0:1], -1
	ds_write2st64_b32 v18, v19, v19 offset0:128 offset1:136
	s_and_saveexec_b64 s[4:5], s[0:1]
	ds_write_b32 v1, v19 offset:4096
	s_or_b64 exec, exec, s[4:5]
	s_and_saveexec_b64 s[4:5], s[0:1]
	v_mov_b32_e32 v19, 0
	ds_write_b32 v1, v19 offset:6144
	s_or_b64 exec, exec, s[4:5]
	s_movk_i32 s0, 0x80
	v_cmp_gt_u32_e64 s[0:1], s0, v0
	s_and_saveexec_b64 s[4:5], s[0:1]
	s_cbranch_execz .LBB4_10
	v_lshlrev_b32_e32 v20, 2, v0
	global_load_dword v19, v20, s[14:15]
	global_load_dword v26, v20, s[14:15] offset:512
	global_load_dword v27, v20, s[14:15] offset:1024
	global_load_dword v28, v20, s[14:15] offset:1536
	global_load_dword v30, v20, s[14:15] offset:2048
	global_load_dword v32, v20, s[14:15] offset:2560
	global_load_dword v34, v20, s[14:15] offset:3072
	global_load_dword v36, v20, s[14:15] offset:3584
	v_mov_b32_e32 v21, 0
	v_lshl_add_u64 v[24:25], s[14:15], 0, v[20:21]
	s_movk_i32 s0, 0x1000
	v_add_co_u32_e64 v24, s[0:1], s0, v24
	s_mov_b32 s3, 0x800000
	s_nop 0
	v_addc_co_u32_e64 v25, s[0:1], 0, v25, s[0:1]
	global_load_dword v38, v[24:25], off
	global_load_dword v39, v[24:25], off offset:512
	global_load_dword v40, v[24:25], off offset:1024
	global_load_dword v41, v[24:25], off offset:1536
	global_load_dword v42, v[24:25], off offset:2048
	global_load_dword v44, v[24:25], off offset:2560
	global_load_dword v46, v[24:25], off offset:3072
	global_load_dword v48, v[24:25], off offset:3584
	global_load_dword v50, v20, s[16:17]
	global_load_dword v51, v20, s[18:19]
	s_mov_b32 s0, 0x88e368f1
	s_mov_b32 s1, 0x3ee4f8b5
	s_waitcnt vmcnt(17)
	v_cvt_f64_f32_e32 v[20:21], v19
	s_waitcnt vmcnt(16)
	v_cvt_f64_f32_e32 v[24:25], v26
	s_waitcnt vmcnt(15)
	v_cvt_f64_f32_e32 v[26:27], v27
	v_add_f64 v[20:21], v[20:21], 0
	s_waitcnt vmcnt(13)
	v_cvt_f64_f32_e32 v[30:31], v30
	v_add_f64 v[20:21], v[20:21], v[26:27]
	v_cvt_f64_f32_e32 v[28:29], v28
	s_waitcnt vmcnt(11)
	v_cvt_f64_f32_e32 v[34:35], v34
	v_add_f64 v[24:25], v[24:25], 0
	v_add_f64 v[20:21], v[20:21], v[30:31]
	v_cvt_f64_f32_e32 v[32:33], v32
	v_add_f64 v[24:25], v[24:25], v[28:29]
	s_waitcnt vmcnt(9)
	v_cvt_f64_f32_e32 v[26:27], v38
	v_add_f64 v[20:21], v[20:21], v[34:35]
	v_cvt_f64_f32_e32 v[36:37], v36
	s_waitcnt vmcnt(8)
	v_cvt_f64_f32_e32 v[28:29], v39
	s_waitcnt vmcnt(7)
	v_cvt_f64_f32_e32 v[38:39], v40
	v_add_f64 v[24:25], v[24:25], v[32:33]
	v_add_f64 v[20:21], v[20:21], v[26:27]
	s_waitcnt vmcnt(5)
	v_cvt_f64_f32_e32 v[42:43], v42
	v_add_f64 v[24:25], v[24:25], v[36:37]
	v_add_f64 v[20:21], v[20:21], v[38:39]
	v_cvt_f64_f32_e32 v[40:41], v41
	s_waitcnt vmcnt(3)
	v_cvt_f64_f32_e32 v[46:47], v46
	v_add_f64 v[24:25], v[24:25], v[28:29]
	v_add_f64 v[20:21], v[20:21], v[42:43]
	v_cvt_f64_f32_e32 v[44:45], v44
	v_add_f64 v[24:25], v[24:25], v[40:41]
	v_add_f64 v[20:21], v[20:21], v[46:47]
	s_waitcnt vmcnt(2)
	v_cvt_f64_f32_e32 v[48:49], v48
	v_add_f64 v[24:25], v[24:25], v[44:45]
	v_mul_f64 v[20:21], v[20:21], s[0:1]
	v_add_f64 v[24:25], v[24:25], v[48:49]
	v_mul_f64 v[26:27], v[20:21], v[20:21]
	v_fma_f64 v[24:25], v[24:25], s[0:1], -v[26:27]
	v_max_f64 v[24:25], v[24:25], 0
	v_cvt_f32_f64_e32 v19, v[24:25]
	v_add_f32_e32 v19, 0x3727c5ac, v19
	v_mul_f32_e32 v24, 0x4b800000, v19
	v_cmp_gt_f32_e64 s[0:1], s3, v19
	v_cvt_f32_f64_e32 v20, v[20:21]
	s_nop 0
	v_cndmask_b32_e64 v19, v19, v24, s[0:1]
	v_rsq_f32_e32 v19, v19
	s_nop 0
	v_mul_f32_e32 v24, 0x45800000, v19
	v_cndmask_b32_e64 v19, v19, v24, s[0:1]
	s_waitcnt vmcnt(1)
	v_mul_f32_e32 v19, v50, v19
	s_waitcnt vmcnt(0)
	v_fma_f32 v20, -v19, v20, v51
	ds_write2st64_b32 v18, v19, v20 offset0:160 offset1:162
.LBB4_10:
	s_or_b64 exec, exec, s[4:5]
	s_waitcnt vmcnt(0)
	s_waitcnt lgkmcnt(0)
	s_barrier
	s_and_saveexec_b64 s[0:1], vcc
	s_cbranch_execz .LBB4_12
	v_lshlrev_b32_e32 v19, 5, v23
	ds_read_b128 v[24:27], v19 offset:40960
	ds_read_b128 v[28:31], v19 offset:40976
	ds_read_b128 v[32:35], v19 offset:41472
	v_lshrrev_b32_e32 v64, 4, v22
	v_and_or_b32 v18, v18, 60, v64
	v_lshlrev_b32_e32 v18, 2, v18
	v_lshlrev_b32_e32 v65, 4, v22
	s_waitcnt lgkmcnt(0)
	v_fma_mix_f32 v20, v24, v14, v32 op_sel_hi:[0,1,0]
	v_fma_mix_f32 v14, v25, v14, v33 op_sel:[0,1,0] op_sel_hi:[0,1,0]
	v_fma_mix_f32 v21, v26, v15, v34 op_sel_hi:[0,1,0]
	v_fma_mix_f32 v15, v27, v15, v35 op_sel:[0,1,0] op_sel_hi:[0,1,0]
	ds_read_b128 v[24:27], v19 offset:41488
	v_max_f32_e32 v20, 0, v20
	v_max_f32_e32 v14, 0, v14
	v_max_f32_e32 v21, 0, v21
	v_max_f32_e32 v15, 0, v15
	s_waitcnt lgkmcnt(0)
	v_fma_mix_f32 v23, v28, v16, v24 op_sel_hi:[0,1,0]
	v_fma_mix_f32 v24, v30, v17, v26 op_sel_hi:[0,1,0]
	v_fma_mix_f32 v17, v31, v17, v27 op_sel:[0,1,0] op_sel_hi:[0,1,0]
	v_max_f32_e32 v24, 0, v24
	v_max_f32_e32 v17, 0, v17
	v_fma_mix_f32 v16, v29, v16, v25 op_sel:[0,1,0] op_sel_hi:[0,1,0]
	v_cvt_pk_f16_f32 v17, v24, v17
	ds_read_b128 v[24:27], v19 offset:41088
	ds_read_b128 v[28:31], v19 offset:41600
	v_cvt_pk_f16_f32 v15, v21, v15
	v_cvt_pk_f16_f32 v14, v20, v14
	v_max_f32_e32 v23, 0, v23
	v_max_f32_e32 v16, 0, v16
	s_waitcnt lgkmcnt(0)
	v_fma_mix_f32 v20, v24, v6, v28 op_sel_hi:[0,1,0]
	v_fma_mix_f32 v6, v25, v6, v29 op_sel:[0,1,0] op_sel_hi:[0,1,0]
	v_fma_mix_f32 v21, v26, v7, v30 op_sel_hi:[0,1,0]
	v_fma_mix_f32 v7, v27, v7, v31 op_sel:[0,1,0] op_sel_hi:[0,1,0]
	ds_read_b128 v[24:27], v19 offset:41104
	ds_read_b128 v[28:31], v19 offset:41616
	v_cvt_pk_f16_f32 v16, v23, v16
	v_max_f32_e32 v20, 0, v20
	v_max_f32_e32 v6, 0, v6
	v_max_f32_e32 v21, 0, v21
	s_waitcnt lgkmcnt(0)
	v_fma_mix_f32 v23, v24, v8, v28 op_sel_hi:[0,1,0]
	v_fma_mix_f32 v24, v26, v9, v30 op_sel_hi:[0,1,0]
	v_fma_mix_f32 v9, v27, v9, v31 op_sel:[0,1,0] op_sel_hi:[0,1,0]
	v_max_f32_e32 v24, 0, v24
	v_max_f32_e32 v9, 0, v9
	v_fma_mix_f32 v8, v25, v8, v29 op_sel:[0,1,0] op_sel_hi:[0,1,0]
	v_cvt_pk_f16_f32 v9, v24, v9
	ds_read_b128 v[24:27], v19 offset:41216
	ds_read_b128 v[28:31], v19 offset:41728
	v_max_f32_e32 v7, 0, v7
	v_cvt_pk_f16_f32 v7, v21, v7
	v_cvt_pk_f16_f32 v6, v20, v6
	v_max_f32_e32 v23, 0, v23
	s_waitcnt lgkmcnt(0)
	v_fma_mix_f32 v20, v24, v10, v28 op_sel_hi:[0,1,0]
	v_fma_mix_f32 v10, v25, v10, v29 op_sel:[0,1,0] op_sel_hi:[0,1,0]
	v_fma_mix_f32 v21, v26, v11, v30 op_sel_hi:[0,1,0]
	v_fma_mix_f32 v11, v27, v11, v31 op_sel:[0,1,0] op_sel_hi:[0,1,0]
	ds_read_b128 v[24:27], v19 offset:41232
	ds_read_b128 v[28:31], v19 offset:41744
	v_max_f32_e32 v8, 0, v8
	v_cvt_pk_f16_f32 v8, v23, v8
	v_max_f32_e32 v20, 0, v20
	v_max_f32_e32 v10, 0, v10
	s_waitcnt lgkmcnt(0)
	v_fma_mix_f32 v23, v24, v12, v28 op_sel_hi:[0,1,0]
	v_fma_mix_f32 v24, v26, v13, v30 op_sel_hi:[0,1,0]
	v_fma_mix_f32 v13, v27, v13, v31 op_sel:[0,1,0] op_sel_hi:[0,1,0]
	v_max_f32_e32 v24, 0, v24
	v_max_f32_e32 v13, 0, v13
	v_fma_mix_f32 v12, v25, v12, v29 op_sel:[0,1,0] op_sel_hi:[0,1,0]
	v_cvt_pk_f16_f32 v13, v24, v13
	ds_read_b128 v[24:27], v19 offset:41344
	ds_read_b128 v[28:31], v19 offset:41856
	v_max_f32_e32 v21, 0, v21
	v_max_f32_e32 v11, 0, v11
	v_cvt_pk_f16_f32 v11, v21, v11
	v_cvt_pk_f16_f32 v10, v20, v10
	s_waitcnt lgkmcnt(0)
	v_fma_mix_f32 v20, v24, v2, v28 op_sel_hi:[0,1,0]
	v_fma_mix_f32 v2, v25, v2, v29 op_sel:[0,1,0] op_sel_hi:[0,1,0]
	v_fma_mix_f32 v21, v26, v3, v30 op_sel_hi:[0,1,0]
	v_fma_mix_f32 v3, v27, v3, v31 op_sel:[0,1,0] op_sel_hi:[0,1,0]
	ds_read_b128 v[24:27], v19 offset:41360
	ds_read_b128 v[28:31], v19 offset:41872
	ds_bpermute_b32 v14, v18, v14
	ds_bpermute_b32 v15, v18, v15
	ds_bpermute_b32 v16, v18, v16
	ds_bpermute_b32 v17, v18, v17
	v_max_f32_e32 v23, 0, v23
	v_max_f32_e32 v12, 0, v12
	v_cvt_pk_f16_f32 v12, v23, v12
	s_waitcnt lgkmcnt(4)
	v_fma_mix_f32 v19, v24, v4, v28 op_sel_hi:[0,1,0]
	v_fma_mix_f32 v4, v25, v4, v29 op_sel:[0,1,0] op_sel_hi:[0,1,0]
	v_fma_mix_f32 v23, v26, v5, v30 op_sel_hi:[0,1,0]
	v_fma_mix_f32 v5, v27, v5, v31 op_sel:[0,1,0] op_sel_hi:[0,1,0]
	v_max_f32_e32 v20, 0, v20
	v_max_f32_e32 v2, 0, v2
	v_max_f32_e32 v21, 0, v21
	v_max_f32_e32 v3, 0, v3
	v_max_f32_e32 v19, 0, v19
	v_max_f32_e32 v4, 0, v4
	v_max_f32_e32 v23, 0, v23
	v_max_f32_e32 v5, 0, v5
	v_cvt_pk_f16_f32 v5, v23, v5
	v_cvt_pk_f16_f32 v4, v19, v4
	v_cvt_pk_f16_f32 v3, v21, v3
	v_cvt_pk_f16_f32 v2, v20, v2
	ds_bpermute_b32 v6, v18, v6
	ds_bpermute_b32 v7, v18, v7
	ds_bpermute_b32 v8, v18, v8
	ds_bpermute_b32 v9, v18, v9
	ds_bpermute_b32 v10, v18, v10
	ds_bpermute_b32 v11, v18, v11
	ds_bpermute_b32 v12, v18, v12
	ds_bpermute_b32 v13, v18, v13
	ds_bpermute_b32 v2, v18, v2
	ds_bpermute_b32 v3, v18, v3
	ds_bpermute_b32 v4, v18, v4
	ds_bpermute_b32 v5, v18, v5
	ds_read_b128 v[18:21], v65
	ds_read_b128 v[22:25], v65 offset:4096
	ds_read_b128 v[26:29], v65 offset:8192
	ds_read_b128 v[42:45], v65 offset:12288
	s_waitcnt lgkmcnt(3)
	v_mfma_f32_16x16x32_f16 v[30:33], v[14:17], v[18:21], 0
	s_waitcnt lgkmcnt(2)
	v_mfma_f32_16x16x32_f16 v[34:37], v[14:17], v[22:25], 0
	ds_read_b128 v[18:21], v65 offset:16384
	ds_read_b128 v[22:25], v65 offset:20480
	ds_read_b128 v[46:49], v65 offset:24576
	ds_read_b128 v[50:53], v65 offset:28672
	s_waitcnt lgkmcnt(5)
	v_mfma_f32_16x16x32_f16 v[38:41], v[14:17], v[26:29], 0
	s_waitcnt lgkmcnt(4)
	v_mfma_f32_16x16x32_f16 v[42:45], v[14:17], v[42:45], 0
	s_waitcnt lgkmcnt(3)
	v_mfma_f32_16x16x32_f16 v[26:29], v[14:17], v[18:21], 0
	s_waitcnt lgkmcnt(2)
	v_mfma_f32_16x16x32_f16 v[22:25], v[14:17], v[22:25], 0
	s_waitcnt lgkmcnt(1)
	v_mfma_f32_16x16x32_f16 v[18:21], v[14:17], v[46:49], 0
	s_waitcnt lgkmcnt(0)
	v_mfma_f32_16x16x32_f16 v[14:17], v[14:17], v[50:53], 0
	ds_read_b128 v[46:49], v65 offset:1024
	ds_read_b128 v[50:53], v65 offset:5120
	ds_read_b128 v[54:57], v65 offset:9216
	ds_read_b128 v[58:61], v65 offset:13312
	s_waitcnt lgkmcnt(3)
	v_mfma_f32_16x16x32_f16 v[30:33], v[6:9], v[46:49], v[30:33]
	s_waitcnt lgkmcnt(2)
	v_mfma_f32_16x16x32_f16 v[34:37], v[6:9], v[50:53], v[34:37]
	s_waitcnt lgkmcnt(1)
	v_mfma_f32_16x16x32_f16 v[38:41], v[6:9], v[54:57], v[38:41]
	s_waitcnt lgkmcnt(0)
	v_mfma_f32_16x16x32_f16 v[42:45], v[6:9], v[58:61], v[42:45]
	ds_read_b128 v[58:61], v65 offset:17408
	ds_read_b128 v[54:57], v65 offset:21504
	ds_read_b128 v[50:53], v65 offset:25600
	ds_read_b128 v[46:49], v65 offset:29696
	s_waitcnt lgkmcnt(3)
	v_mfma_f32_16x16x32_f16 v[26:29], v[6:9], v[58:61], v[26:29]
	s_waitcnt lgkmcnt(2)
	v_mfma_f32_16x16x32_f16 v[22:25], v[6:9], v[54:57], v[22:25]
	s_waitcnt lgkmcnt(1)
	v_mfma_f32_16x16x32_f16 v[18:21], v[6:9], v[50:53], v[18:21]
	s_waitcnt lgkmcnt(0)
	v_mfma_f32_16x16x32_f16 v[14:17], v[6:9], v[46:49], v[14:17]
	ds_read_b128 v[6:9], v65 offset:2048
	ds_read_b128 v[46:49], v65 offset:6144
	ds_read_b128 v[50:53], v65 offset:10240
	ds_read_b128 v[54:57], v65 offset:14336
	s_waitcnt lgkmcnt(3)
	v_mfma_f32_16x16x32_f16 v[30:33], v[10:13], v[6:9], v[30:33]
	s_waitcnt lgkmcnt(2)
	v_mfma_f32_16x16x32_f16 v[46:49], v[10:13], v[46:49], v[34:37]
	s_waitcnt lgkmcnt(1)
	v_mfma_f32_16x16x32_f16 v[50:53], v[10:13], v[50:53], v[38:41]
	s_waitcnt lgkmcnt(0)
	v_mfma_f32_16x16x32_f16 v[42:45], v[10:13], v[54:57], v[42:45]
	ds_read_b128 v[6:9], v65 offset:18432
	ds_read_b128 v[34:37], v65 offset:22528
	ds_read_b128 v[38:41], v65 offset:26624
	ds_read_b128 v[54:57], v65 offset:30720
	s_waitcnt lgkmcnt(3)
	v_mfma_f32_16x16x32_f16 v[6:9], v[10:13], v[6:9], v[26:29]
	s_waitcnt lgkmcnt(2)
	v_mfma_f32_16x16x32_f16 v[26:29], v[10:13], v[34:37], v[22:25]
	s_waitcnt lgkmcnt(1)
	v_mfma_f32_16x16x32_f16 v[34:37], v[10:13], v[38:41], v[18:21]
	s_waitcnt lgkmcnt(0)
	v_mfma_f32_16x16x32_f16 v[38:41], v[10:13], v[54:57], v[14:17]
	ds_read_b128 v[10:13], v65 offset:3072
	s_nop 1
	ds_read_b128 v[14:17], v65 offset:7168
	ds_read_b128 v[54:57], v65 offset:11264
	ds_read_b128 v[58:61], v65 offset:15360
	s_waitcnt lgkmcnt(3)
	v_mfma_f32_16x16x32_f16 v[22:25], v[2:5], v[10:13], v[30:33]
	s_waitcnt lgkmcnt(2)
	v_mfma_f32_16x16x32_f16 v[18:21], v[2:5], v[14:17], v[46:49]
	s_waitcnt lgkmcnt(1)
	v_mfma_f32_16x16x32_f16 v[14:17], v[2:5], v[54:57], v[50:53]
	s_waitcnt lgkmcnt(0)
	v_mfma_f32_16x16x32_f16 v[10:13], v[2:5], v[58:61], v[42:45]
	ds_read_b128 v[30:33], v65 offset:19456
	s_nop 1
	ds_read_b128 v[42:45], v65 offset:23552
	ds_read_b128 v[46:49], v65 offset:27648
	ds_read_b128 v[50:53], v65 offset:31744
	v_lshlrev_b32_e32 v59, 2, v64
	v_lshlrev_b32_e32 v58, 10, v62
	s_waitcnt lgkmcnt(3)
	v_mfma_f32_16x16x32_f16 v[30:33], v[2:5], v[30:33], v[6:9]
	s_waitcnt lgkmcnt(1)
	v_mfma_f32_16x16x32_f16 v[6:9], v[2:5], v[46:49], v[34:37]
	s_nop 2
	v_lshlrev_b32_e32 v34, 3, v0
	v_mfma_f32_16x16x32_f16 v[26:29], v[2:5], v[42:45], v[26:29]
	v_and_b32_e32 v44, 0x78, v34
	v_lshlrev_b32_e32 v34, 4, v63
	v_ashrrev_i32_e32 v35, 31, v34
	v_lshl_add_u64 v[36:37], v[34:35], 2, s[8:9]
	v_and_b32_e32 v42, 48, v0
	v_mov_b32_e32 v43, 0
	v_lshl_add_u64 v[36:37], v[36:37], 0, v[42:43]
	v_lshlrev_b32_e32 v42, 1, v44
	v_lshlrev_b32_e32 v60, 2, v44
	s_waitcnt lgkmcnt(0)
	v_mfma_f32_16x16x32_f16 v[2:5], v[2:5], v[50:53], v[38:41]
	v_or_b32_e32 v48, v34, v59
	v_lshl_add_u64 v[46:47], s[12:13], 0, v[42:43]
	v_mov_b32_e32 v52, v14
	global_load_dwordx4 v[38:41], v[36:37], off
	s_nop 0
	global_load_dwordx4 v[34:37], v60, s[6:7] offset:16
	global_load_dwordx4 v[42:45], v60, s[6:7]
	v_mov_b32_e32 v53, v10
	v_mov_b32_e32 v50, v22
	v_mov_b32_e32 v51, v18
	v_ashrrev_i32_e32 v49, 31, v48
	v_mov_b32_e32 v18, v23
	v_mov_b32_e32 v10, v15
	v_lshlrev_b64 v[66:67], 8, v[48:49]
	v_lshl_add_u64 v[66:67], v[46:47], 0, v[66:67]
	s_waitcnt vmcnt(0)
	v_pk_add_f32 v[52:53], v[44:45], v[52:53]
	s_nop 0
	v_pk_mul_f32 v[54:55], v[38:39], v[52:53] op_sel_hi:[0,1]
	v_mov_b32_e32 v52, v30
	v_mov_b32_e32 v53, v26
	v_pk_add_f32 v[52:53], v[34:35], v[52:53]
	v_pk_add_f32 v[50:51], v[42:43], v[50:51]
	v_pk_mul_f32 v[56:57], v[38:39], v[52:53] op_sel_hi:[0,1]
	v_mov_b32_e32 v52, v6
	v_mov_b32_e32 v53, v2
	v_pk_add_f32 v[52:53], v[36:37], v[52:53]
	v_mov_b32_e32 v26, v31
	v_mov_b32_e32 v2, v7
	v_or_b32_e32 v6, 1, v48
	v_pk_mul_f32 v[50:51], v[38:39], v[50:51] op_sel_hi:[0,1]
	v_pk_mul_f32 v[52:53], v[38:39], v[52:53] op_sel_hi:[0,1]
	v_pk_add_f32 v[18:19], v[42:43], v[18:19]
	v_pk_add_f32 v[10:11], v[44:45], v[10:11]
	v_pk_add_f32 v[14:15], v[34:35], v[26:27]
	v_pk_add_f32 v[2:3], v[36:37], v[2:3]
	v_ashrrev_i32_e32 v7, 31, v6
	v_cvt_pk_f16_f32 v62, v50, v51
	v_cvt_pk_f16_f32 v63, v54, v55
	v_cvt_pk_f16_f32 v64, v56, v57
	v_cvt_pk_f16_f32 v65, v52, v53
	v_pk_mul_f32 v[18:19], v[38:39], v[18:19] op_sel:[1,0]
	v_pk_mul_f32 v[10:11], v[38:39], v[10:11] op_sel:[1,0]
	v_pk_mul_f32 v[22:23], v[38:39], v[14:15] op_sel:[1,0]
	v_pk_mul_f32 v[2:3], v[38:39], v[2:3] op_sel:[1,0]
	v_lshlrev_b64 v[6:7], 8, v[6:7]
	global_store_dwordx4 v[66:67], v[62:65], off sc0 sc1
	v_lshl_add_u64 v[6:7], v[46:47], 0, v[6:7]
	s_nop 0
	v_cvt_pk_f16_f32 v62, v18, v19
	v_cvt_pk_f16_f32 v63, v10, v11
	v_cvt_pk_f16_f32 v64, v22, v23
	v_cvt_pk_f16_f32 v65, v2, v3
	global_store_dwordx4 v[6:7], v[62:65], off sc0 sc1
	v_mov_b32_e32 v6, v24
	v_mov_b32_e32 v7, v20
	v_pk_add_f32 v[6:7], v[42:43], v[6:7]
	v_mov_b32_e32 v20, v25
	v_pk_mul_f32 v[14:15], v[40:41], v[6:7] op_sel_hi:[0,1]
	v_mov_b32_e32 v6, v16
	v_mov_b32_e32 v7, v12
	v_pk_add_f32 v[6:7], v[44:45], v[6:7]
	v_mov_b32_e32 v12, v17
	v_pk_mul_f32 v[30:31], v[40:41], v[6:7] op_sel_hi:[0,1]
	v_mov_b32_e32 v6, v32
	v_mov_b32_e32 v7, v28
	v_pk_add_f32 v[6:7], v[34:35], v[6:7]
	v_mov_b32_e32 v16, v41
	v_pk_mul_f32 v[38:39], v[40:41], v[6:7] op_sel_hi:[0,1]
	v_mov_b32_e32 v6, v8
	v_mov_b32_e32 v7, v4
	v_pk_add_f32 v[6:7], v[36:37], v[6:7]
	v_pk_add_f32 v[12:13], v[44:45], v[12:13]
	v_pk_mul_f32 v[26:27], v[40:41], v[6:7] op_sel_hi:[0,1]
	v_or_b32_e32 v6, 2, v48
	v_ashrrev_i32_e32 v7, 31, v6
	v_lshlrev_b64 v[6:7], 8, v[6:7]
	v_mov_b32_e32 v28, v33
	v_cvt_pk_f16_f32 v62, v14, v15
	v_cvt_pk_f16_f32 v63, v30, v31
	v_cvt_pk_f16_f32 v64, v38, v39
	v_cvt_pk_f16_f32 v65, v26, v27
	v_lshl_add_u64 v[6:7], v[46:47], 0, v[6:7]
	v_pk_mul_f32 v[24:25], v[16:17], v[12:13] op_sel_hi:[0,1]
	v_pk_add_f32 v[12:13], v[34:35], v[28:29]
	v_add_f32_e32 v4, 0, v52
	global_store_dwordx4 v[6:7], v[62:65], off sc0 sc1
	v_pk_add_f32 v[6:7], v[42:43], v[20:21]
	v_pk_mul_f32 v[28:29], v[16:17], v[12:13] op_sel_hi:[0,1]
	v_pk_mul_f32 v[12:13], v[2:3], v[2:3]
	v_add_f32_e32 v2, v2, v4
	v_pk_mul_f32 v[20:21], v[16:17], v[6:7] op_sel_hi:[0,1]
	v_add_f32_e32 v17, v26, v2
	v_add_f32_e32 v2, 0, v57
	v_add_f32_e32 v2, v23, v2
	v_pk_fma_f32 v[12:13], v[52:53], v[52:53], v[12:13]
	v_add_f32_e32 v2, v39, v2
	v_pk_fma_f32 v[32:33], v[26:27], v[26:27], v[12:13]
	v_pk_mul_f32 v[12:13], v[22:23], v[22:23]
	v_add_f32_e32 v26, v29, v2
	v_add_f32_e32 v2, 0, v56
	v_pk_fma_f32 v[12:13], v[56:57], v[56:57], v[12:13]
	v_add_f32_e32 v2, v22, v2
	v_pk_fma_f32 v[12:13], v[38:39], v[38:39], v[12:13]
	v_add_f32_e32 v2, v38, v2
	v_cvt_pk_f16_f32 v8, v28, v29
	v_pk_fma_f32 v[12:13], v[28:29], v[28:29], v[12:13]
	v_add_f32_e32 v28, v28, v2
	v_pk_mul_f32 v[22:23], v[10:11], v[10:11]
	v_add_f32_e32 v2, 0, v55
	v_pk_fma_f32 v[22:23], v[54:55], v[54:55], v[22:23]
	v_add_f32_e32 v2, v11, v2
	v_pk_fma_f32 v[22:23], v[30:31], v[30:31], v[22:23]
	v_add_f32_e32 v2, v31, v2
	v_cvt_pk_f16_f32 v7, v24, v25
	v_pk_fma_f32 v[22:23], v[24:25], v[24:25], v[22:23]
	v_add_f32_e32 v25, v25, v2
	v_add_f32_e32 v2, 0, v54
	v_add_f32_e32 v2, v10, v2
	v_add_f32_e32 v2, v30, v2
	v_add_f32_e32 v24, v24, v2
	v_add_f32_e32 v2, 0, v51
	v_pk_mul_f32 v[10:11], v[18:19], v[18:19]
	v_add_f32_e32 v2, v19, v2
	v_pk_fma_f32 v[10:11], v[50:51], v[50:51], v[10:11]
	v_add_f32_e32 v2, v15, v2
	v_pk_fma_f32 v[10:11], v[14:15], v[14:15], v[10:11]
	v_add_f32_e32 v15, v21, v2
	v_add_f32_e32 v2, 0, v50
	v_add_f32_e32 v2, v18, v2
	v_add_f32_e32 v2, v14, v2
	v_add_f32_e32 v14, v20, v2
	v_add_f32_e32 v2, 0, v53
	v_add_f32_e32 v2, v3, v2
	v_mov_b32_e32 v4, v9
	v_add_f32_e32 v18, v27, v2
	v_pk_add_f32 v[2:3], v[36:37], v[4:5]
	v_cvt_pk_f16_f32 v6, v20, v21
	v_pk_mul_f32 v[2:3], v[16:17], v[2:3] op_sel_hi:[0,1]
	v_cvt_pk_f16_f32 v9, v2, v3
	v_pk_fma_f32 v[4:5], v[2:3], v[2:3], v[32:33]
	v_add_f32_e32 v16, v2, v17
	v_or_b32_e32 v2, 3, v48
	v_add_f32_e32 v17, v3, v18
	v_ashrrev_i32_e32 v3, 31, v2
	v_lshlrev_b64 v[2:3], 8, v[2:3]
	v_lshl_add_u64 v[2:3], v[46:47], 0, v[2:3]
	v_permlane16_swap_b32_e32 v14, v15
	v_permlane16_swap_b32_e32 v24, v25
	global_store_dwordx4 v[2:3], v[6:9], off sc0 sc1
	v_add_f32_e32 v2, v14, v15
	v_add_f32_e32 v3, v24, v25
	v_permlane16_swap_b32_e32 v28, v26
	v_permlane16_swap_b32_e32 v16, v17
	v_permlane32_swap_b32_e32 v2, v3
	v_add_f32_e32 v6, v28, v26
	v_add_f32_e32 v7, v16, v17
	v_add_f32_e32 v2, v2, v3
	v_or3_b32 v3, v58, v60, v59
	v_permlane32_swap_b32_e32 v6, v7
	v_pk_fma_f32 v[10:11], v[20:21], v[20:21], v[10:11]
	v_add_f32_e32 v6, v6, v7
	v_add_u32_e32 v3, 0x8000, v3
	ds_write2_b32 v3, v2, v6 offset1:4
	v_mov_b32_e32 v2, v11
	v_mov_b32_e32 v6, v23
	s_nop 0
	v_permlane16_swap_b32_e32 v10, v2
	v_permlane16_swap_b32_e32 v22, v6
	v_add_f32_e32 v2, v10, v2
	v_add_f32_e32 v6, v22, v6
	s_nop 1
	v_permlane32_swap_b32_e32 v2, v6
	v_add_f32_e32 v2, v2, v6
	v_mov_b32_e32 v6, v13
	s_nop 1
	v_permlane16_swap_b32_e32 v12, v6
	v_permlane16_swap_b32_e32 v4, v5
	v_add_f32_e32 v6, v12, v6
	v_add_f32_e32 v4, v4, v5
	s_nop 1
	v_permlane32_swap_b32_e32 v6, v4
	v_add_f32_e32 v4, v6, v4
	ds_write2_b32 v3, v2, v4 offset0:128 offset1:132
